# speedup vs baseline: 1.0454x; 1.0029x over previous
.LBB1_65:
	s_or_b64 exec, exec, s[2:3]
	s_waitcnt lgkmcnt(0)
	s_barrier
	ds_read2st64_b32 v[76:77], v223 offset1:2
	v_add_u32_e32 v67, v222, v224
	s_cmp_eq_u64 s[6:7], 0
	s_cbranch_scc0 .Lep1_k1
	v_mov_b32_e32 v18, 0
	v_mov_b32_e32 v19, 0
	v_mov_b32_e32 v20, 0
	v_mov_b32_e32 v21, 0
	ds_read2st64_b32 v[50:51], v221 offset0:0 offset1:1
	ds_read2st64_b32 v[52:53], v221 offset0:2 offset1:3
	ds_read2st64_b32 v[54:55], v221 offset0:4 offset1:5
	ds_read2st64_b32 v[56:57], v221 offset0:6 offset1:7
	ds_read2st64_b32 v[58:59], v221 offset0:8 offset1:9
	ds_read2st64_b32 v[60:61], v221 offset0:10 offset1:11
	ds_read2st64_b32 v[62:63], v67 offset0:0 offset1:2
	ds_read2st64_b32 v[64:65], v67 offset0:4 offset1:6
	ds_read2st64_b32 v[68:69], v67 offset0:16 offset1:18
	ds_read2st64_b32 v[70:71], v67 offset0:20 offset1:22
	ds_read2st64_b32 v[72:73], v67 offset0:32 offset1:34
	ds_read2st64_b32 v[74:75], v67 offset0:36 offset1:38
	s_waitcnt lgkmcnt(12)
	v_fma_f32 v78, -v76, v77, 0
	s_waitcnt lgkmcnt(4)
	v_pk_add_f32 v[34:35], v[34:35], v[50:51]
	v_pk_add_f32 v[36:37], v[36:37], v[52:53]
	v_pk_add_f32 v[34:35], v[34:35], v[78:79] op_sel_hi:[1,0]
	v_pk_add_f32 v[36:37], v[36:37], v[78:79] op_sel_hi:[1,0]
	v_pk_fma_f32 v[34:35], v[62:63], v[76:77], v[34:35] op_sel:[0,1,0] op_sel_hi:[1,1,1]
	v_pk_fma_f32 v[36:37], v[64:65], v[76:77], v[36:37] op_sel:[0,1,0] op_sel_hi:[1,1,1]
	v_pk_add_f32 v[18:19], v[18:19], v[34:35]
	v_pk_fma_f32 v[20:21], v[34:35], v[34:35], v[20:21]
	v_pk_add_f32 v[18:19], v[18:19], v[36:37]
	v_pk_fma_f32 v[20:21], v[36:37], v[36:37], v[20:21]
	s_waitcnt lgkmcnt(2)
	v_pk_add_f32 v[38:39], v[38:39], v[54:55]
	v_pk_add_f32 v[40:41], v[40:41], v[56:57]
	v_pk_add_f32 v[38:39], v[38:39], v[78:79] op_sel_hi:[1,0]
	v_pk_add_f32 v[40:41], v[40:41], v[78:79] op_sel_hi:[1,0]
	v_pk_fma_f32 v[38:39], v[68:69], v[76:77], v[38:39] op_sel:[0,1,0] op_sel_hi:[1,1,1]
	v_pk_fma_f32 v[40:41], v[70:71], v[76:77], v[40:41] op_sel:[0,1,0] op_sel_hi:[1,1,1]
	v_pk_add_f32 v[18:19], v[18:19], v[38:39]
	v_pk_fma_f32 v[20:21], v[38:39], v[38:39], v[20:21]
	v_pk_add_f32 v[18:19], v[18:19], v[40:41]
	v_pk_fma_f32 v[20:21], v[40:41], v[40:41], v[20:21]
	s_waitcnt lgkmcnt(0)
	v_pk_add_f32 v[42:43], v[42:43], v[58:59]
	v_pk_add_f32 v[44:45], v[44:45], v[60:61]
	v_pk_add_f32 v[42:43], v[42:43], v[78:79] op_sel_hi:[1,0]
	v_pk_add_f32 v[44:45], v[44:45], v[78:79] op_sel_hi:[1,0]
	v_pk_fma_f32 v[42:43], v[72:73], v[76:77], v[42:43] op_sel:[0,1,0] op_sel_hi:[1,1,1]
	v_pk_fma_f32 v[44:45], v[74:75], v[76:77], v[44:45] op_sel:[0,1,0] op_sel_hi:[1,1,1]
	v_pk_add_f32 v[18:19], v[18:19], v[42:43]
	v_pk_fma_f32 v[20:21], v[42:43], v[42:43], v[20:21]
	v_pk_add_f32 v[18:19], v[18:19], v[44:45]
	v_pk_fma_f32 v[20:21], v[44:45], v[44:45], v[20:21]
	ds_read2st64_b32 v[50:51], v221 offset0:12 offset1:13
	ds_read2st64_b32 v[52:53], v221 offset0:14 offset1:15
	ds_read2st64_b32 v[54:55], v221 offset0:16 offset1:17
	ds_read2st64_b32 v[56:57], v221 offset0:18 offset1:19
	ds_read2st64_b32 v[58:59], v221 offset0:20 offset1:21
	ds_read2st64_b32 v[60:61], v221 offset0:22 offset1:23
	ds_read2st64_b32 v[62:63], v67 offset0:48 offset1:50
	ds_read2st64_b32 v[64:65], v67 offset0:52 offset1:54
	ds_read2st64_b32 v[68:69], v67 offset0:64 offset1:66
	ds_read2st64_b32 v[70:71], v67 offset0:68 offset1:70
	ds_read2st64_b32 v[72:73], v67 offset0:80 offset1:82
	ds_read2st64_b32 v[74:75], v67 offset0:84 offset1:86
	s_barrier
	ds_read_b32 v80, v236
	s_waitcnt lgkmcnt(5)
	v_pk_add_f32 v[46:47], v[46:47], v[50:51]
	v_pk_add_f32 v[48:49], v[48:49], v[52:53]
	v_pk_add_f32 v[46:47], v[46:47], v[78:79] op_sel_hi:[1,0]
	v_pk_add_f32 v[48:49], v[48:49], v[78:79] op_sel_hi:[1,0]
	v_pk_fma_f32 v[46:47], v[62:63], v[76:77], v[46:47] op_sel:[0,1,0] op_sel_hi:[1,1,1]
	v_pk_fma_f32 v[48:49], v[64:65], v[76:77], v[48:49] op_sel:[0,1,0] op_sel_hi:[1,1,1]
	v_pk_add_f32 v[18:19], v[18:19], v[46:47]
	v_pk_fma_f32 v[20:21], v[46:47], v[46:47], v[20:21]
	v_pk_add_f32 v[18:19], v[18:19], v[48:49]
	v_pk_fma_f32 v[20:21], v[48:49], v[48:49], v[20:21]
	s_waitcnt lgkmcnt(3)
	v_pk_add_f32 v[2:3], v[2:3], v[54:55]
	v_pk_add_f32 v[4:5], v[4:5], v[56:57]
	v_pk_add_f32 v[2:3], v[2:3], v[78:79] op_sel_hi:[1,0]
	v_pk_add_f32 v[4:5], v[4:5], v[78:79] op_sel_hi:[1,0]
	v_pk_fma_f32 v[2:3], v[68:69], v[76:77], v[2:3] op_sel:[0,1,0] op_sel_hi:[1,1,1]
	v_pk_fma_f32 v[4:5], v[70:71], v[76:77], v[4:5] op_sel:[0,1,0] op_sel_hi:[1,1,1]
	v_pk_add_f32 v[18:19], v[18:19], v[2:3]
	v_pk_fma_f32 v[20:21], v[2:3], v[2:3], v[20:21]
	v_pk_add_f32 v[18:19], v[18:19], v[4:5]
	v_pk_fma_f32 v[20:21], v[4:5], v[4:5], v[20:21]
	s_waitcnt lgkmcnt(1)
	v_pk_add_f32 v[6:7], v[6:7], v[58:59]
	v_pk_add_f32 v[8:9], v[8:9], v[60:61]
	v_pk_add_f32 v[6:7], v[6:7], v[78:79] op_sel_hi:[1,0]
	v_pk_add_f32 v[8:9], v[8:9], v[78:79] op_sel_hi:[1,0]
	v_pk_fma_f32 v[6:7], v[72:73], v[76:77], v[6:7] op_sel:[0,1,0] op_sel_hi:[1,1,1]
	v_pk_fma_f32 v[8:9], v[74:75], v[76:77], v[8:9] op_sel:[0,1,0] op_sel_hi:[1,1,1]
	v_pk_add_f32 v[18:19], v[18:19], v[6:7]
	v_pk_fma_f32 v[20:21], v[6:7], v[6:7], v[20:21]
	v_pk_add_f32 v[18:19], v[18:19], v[8:9]
	v_pk_fma_f32 v[20:21], v[8:9], v[8:9], v[20:21]
	v_add_f32_e32 v18, v18, v19
	v_add_f32_e32 v20, v20, v21
	v_mov_b32_e32 v19, v18
	v_mov_b32_e32 v21, v20
	s_nop 1
	v_permlane32_swap_b32_e32 v18, v19
	v_permlane32_swap_b32_e32 v20, v21
	v_add_f32_e32 v18, v18, v19
	v_add_f32_e32 v20, v20, v21
	v_cndmask_b32_e64 v22, v20, v18, s[0:1]
	s_branch .Lep1_wr0
.Lep1_k1:
	s_setprio 2
	v_mov_b32_e32 v34, 0
	v_mov_b32_e32 v35, 0
	v_mov_b32_e32 v36, 0
	v_mov_b32_e32 v37, 0
	ds_read2st64_b32 v[50:51], v221 offset0:24 offset1:25
	ds_read2st64_b32 v[52:53], v221 offset0:26 offset1:27
	ds_read2st64_b32 v[54:55], v221 offset0:28 offset1:29
	ds_read2st64_b32 v[56:57], v221 offset0:30 offset1:31
	ds_read2st64_b32 v[58:59], v221 offset0:32 offset1:33
	ds_read2st64_b32 v[60:61], v221 offset0:34 offset1:35
	ds_read2st64_b32 v[62:63], v67 offset0:96 offset1:98
	ds_read2st64_b32 v[64:65], v67 offset0:100 offset1:102
	ds_read2st64_b32 v[68:69], v67 offset0:112 offset1:114
	ds_read2st64_b32 v[70:71], v67 offset0:116 offset1:118
	ds_read2st64_b32 v[72:73], v67 offset0:128 offset1:130
	ds_read2st64_b32 v[74:75], v67 offset0:132 offset1:134
	s_waitcnt lgkmcnt(12)
	v_fma_f32 v78, -v76, v77, 0
	s_waitcnt lgkmcnt(4)
	v_pk_add_f32 v[10:11], v[10:11], v[50:51]
	v_pk_add_f32 v[12:13], v[12:13], v[52:53]
	v_pk_add_f32 v[10:11], v[10:11], v[78:79] op_sel_hi:[1,0]
	v_pk_add_f32 v[12:13], v[12:13], v[78:79] op_sel_hi:[1,0]
	v_pk_fma_f32 v[10:11], v[62:63], v[76:77], v[10:11] op_sel:[0,1,0] op_sel_hi:[1,1,1]
	v_pk_fma_f32 v[12:13], v[64:65], v[76:77], v[12:13] op_sel:[0,1,0] op_sel_hi:[1,1,1]
	v_pk_add_f32 v[34:35], v[34:35], v[10:11]
	v_pk_fma_f32 v[36:37], v[10:11], v[10:11], v[36:37]
	v_pk_add_f32 v[34:35], v[34:35], v[12:13]
	v_pk_fma_f32 v[36:37], v[12:13], v[12:13], v[36:37]
	s_waitcnt lgkmcnt(2)
	v_pk_add_f32 v[14:15], v[14:15], v[54:55]
	v_pk_add_f32 v[16:17], v[16:17], v[56:57]
	v_pk_add_f32 v[14:15], v[14:15], v[78:79] op_sel_hi:[1,0]
	v_pk_add_f32 v[16:17], v[16:17], v[78:79] op_sel_hi:[1,0]
	v_pk_fma_f32 v[14:15], v[68:69], v[76:77], v[14:15] op_sel:[0,1,0] op_sel_hi:[1,1,1]
	v_pk_fma_f32 v[16:17], v[70:71], v[76:77], v[16:17] op_sel:[0,1,0] op_sel_hi:[1,1,1]
	v_pk_add_f32 v[34:35], v[34:35], v[14:15]
	v_pk_fma_f32 v[36:37], v[14:15], v[14:15], v[36:37]
	v_pk_add_f32 v[34:35], v[34:35], v[16:17]
	v_pk_fma_f32 v[36:37], v[16:17], v[16:17], v[36:37]
	s_waitcnt lgkmcnt(0)
	v_pk_add_f32 v[18:19], v[18:19], v[58:59]
	v_pk_add_f32 v[20:21], v[20:21], v[60:61]
	v_pk_add_f32 v[18:19], v[18:19], v[78:79] op_sel_hi:[1,0]
	v_pk_add_f32 v[20:21], v[20:21], v[78:79] op_sel_hi:[1,0]
	v_pk_fma_f32 v[18:19], v[72:73], v[76:77], v[18:19] op_sel:[0,1,0] op_sel_hi:[1,1,1]
	v_pk_fma_f32 v[20:21], v[74:75], v[76:77], v[20:21] op_sel:[0,1,0] op_sel_hi:[1,1,1]
	v_pk_add_f32 v[34:35], v[34:35], v[18:19]
	v_pk_fma_f32 v[36:37], v[18:19], v[18:19], v[36:37]
	v_pk_add_f32 v[34:35], v[34:35], v[20:21]
	v_pk_fma_f32 v[36:37], v[20:21], v[20:21], v[36:37]
	ds_read2st64_b32 v[50:51], v221 offset0:36 offset1:37
	ds_read2st64_b32 v[52:53], v221 offset0:38 offset1:39
	ds_read2st64_b32 v[62:63], v67 offset0:144 offset1:146
	ds_read2st64_b32 v[64:65], v67 offset0:148 offset1:150
	s_waitcnt lgkmcnt(0)
	v_pk_add_f32 v[22:23], v[22:23], v[50:51]
	v_pk_add_f32 v[24:25], v[24:25], v[52:53]
	v_pk_add_f32 v[22:23], v[22:23], v[78:79] op_sel_hi:[1,0]
	v_pk_add_f32 v[24:25], v[24:25], v[78:79] op_sel_hi:[1,0]
	v_pk_fma_f32 v[22:23], v[62:63], v[76:77], v[22:23] op_sel:[0,1,0] op_sel_hi:[1,1,1]
	v_pk_fma_f32 v[24:25], v[64:65], v[76:77], v[24:25] op_sel:[0,1,0] op_sel_hi:[1,1,1]
	v_pk_add_f32 v[34:35], v[34:35], v[22:23]
	v_pk_fma_f32 v[36:37], v[22:23], v[22:23], v[36:37]
	v_pk_add_f32 v[34:35], v[34:35], v[24:25]
	v_pk_fma_f32 v[36:37], v[24:25], v[24:25], v[36:37]
	s_mov_b64 s[40:41], exec
	s_and_b64 exec, exec, s[0:1]
	ds_read2st64_b32 v[50:51], v221 offset0:40 offset1:41
	ds_read2st64_b32 v[52:53], v221 offset0:42 offset1:43
	ds_read2st64_b32 v[62:63], v67 offset0:160 offset1:162
	ds_read2st64_b32 v[64:65], v67 offset0:164 offset1:166
	s_waitcnt lgkmcnt(0)
	v_pk_add_f32 v[26:27], v[26:27], v[50:51]
	v_pk_add_f32 v[28:29], v[28:29], v[52:53]
	v_pk_add_f32 v[26:27], v[26:27], v[78:79] op_sel_hi:[1,0]
	v_pk_add_f32 v[28:29], v[28:29], v[78:79] op_sel_hi:[1,0]
	v_pk_fma_f32 v[26:27], v[62:63], v[76:77], v[26:27] op_sel:[0,1,0] op_sel_hi:[1,1,1]
	v_pk_fma_f32 v[28:29], v[64:65], v[76:77], v[28:29] op_sel:[0,1,0] op_sel_hi:[1,1,1]
	v_pk_add_f32 v[34:35], v[34:35], v[26:27]
	v_pk_fma_f32 v[36:37], v[26:27], v[26:27], v[36:37]
	v_pk_add_f32 v[34:35], v[34:35], v[28:29]
	v_pk_fma_f32 v[36:37], v[28:29], v[28:29], v[36:37]
	s_mov_b64 exec, s[40:41]
	v_add_f32_e32 v34, v34, v35
	v_add_f32_e32 v36, v36, v37
	v_mov_b32_e32 v35, v34
	v_mov_b32_e32 v37, v36
	s_nop 1
	v_permlane32_swap_b32_e32 v34, v35
	v_permlane32_swap_b32_e32 v36, v37
	v_add_f32_e32 v34, v34, v35
	v_add_f32_e32 v36, v36, v37
	v_cndmask_b32_e64 v38, v36, v34, s[0:1]
	ds_write_b32 v236, v38
.Lep1_join:
	s_waitcnt lgkmcnt(0)
	s_barrier
	s_setprio 0
	s_branch .Lep1_w1
.Lep1_wr0:
	s_mul_i32 s43, s36, 0x5000
	s_add_i32 s43, s43, s86
	s_add_u32 s40, s18, s43
	s_addc_u32 s41, s19, 0
	s_waitcnt lgkmcnt(0)
	v_add_f32_e32 v22, v22, v80
	v_mov_b32_e32 v59, v22
	v_cndmask_b32_e64 v57, v22, 1.0, s[84:85]
	v_writelane_b32 v59, 1.0, 0
	s_mov_b64 s[44:45], exec
	s_mov_b32 exec_lo, -1
	s_mov_b32 exec_hi, 0xfffffff
	global_atomic_add_f32 v253, v57, s[40:41]
	s_mov_b32 exec_lo, 0xf0000001
	s_mov_b32 exec_hi, 0xf0000000
	global_atomic_add_f32 v254, v59, s[40:41]
	s_mov_b64 exec, s[44:45]
	ds_write2st64_b32 v67, v34, v35 offset0:0 offset1:2
	ds_write2st64_b32 v67, v36, v37 offset0:4 offset1:6
	ds_write2st64_b32 v67, v38, v39 offset0:16 offset1:18
	ds_write2st64_b32 v67, v40, v41 offset0:20 offset1:22
	ds_write2st64_b32 v67, v42, v43 offset0:32 offset1:34
	ds_write2st64_b32 v67, v44, v45 offset0:36 offset1:38
	ds_write2st64_b32 v67, v46, v47 offset0:48 offset1:50
	ds_write2st64_b32 v67, v48, v49 offset0:52 offset1:54
	ds_write2st64_b32 v67, v2, v3 offset0:64 offset1:66
	ds_write2st64_b32 v67, v4, v5 offset0:68 offset1:70
	ds_write2st64_b32 v67, v6, v7 offset0:80 offset1:82
	ds_write2st64_b32 v67, v8, v9 offset0:84 offset1:86
	s_branch .Lep1_end

.LBB1_146:
	s_or_b64 exec, exec, s[2:3]
	s_waitcnt lgkmcnt(0)
	s_barrier
	ds_read2st64_b32 v[76:77], v223 offset1:2
	v_add_u32_e32 v67, v222, v224
	s_cmp_eq_u64 s[6:7], 0
	s_cbranch_scc0 .Lep2_k1
	v_mov_b32_e32 v18, 0
	v_mov_b32_e32 v19, 0
	v_mov_b32_e32 v20, 0
	v_mov_b32_e32 v21, 0
	ds_read2st64_b32 v[50:51], v221 offset0:0 offset1:1
	ds_read2st64_b32 v[52:53], v221 offset0:2 offset1:3
	ds_read2st64_b32 v[54:55], v221 offset0:4 offset1:5
	ds_read2st64_b32 v[56:57], v221 offset0:6 offset1:7
	ds_read2st64_b32 v[58:59], v221 offset0:8 offset1:9
	ds_read2st64_b32 v[60:61], v221 offset0:10 offset1:11
	ds_read2st64_b32 v[62:63], v67 offset0:0 offset1:2
	ds_read2st64_b32 v[64:65], v67 offset0:4 offset1:6
	ds_read2st64_b32 v[68:69], v67 offset0:16 offset1:18
	ds_read2st64_b32 v[70:71], v67 offset0:20 offset1:22
	ds_read2st64_b32 v[72:73], v67 offset0:32 offset1:34
	ds_read2st64_b32 v[74:75], v67 offset0:36 offset1:38
	s_waitcnt lgkmcnt(12)
	v_fma_f32 v78, -v76, v77, v173
	s_waitcnt lgkmcnt(4)
	v_pk_add_f32 v[34:35], v[34:35], v[50:51]
	v_pk_add_f32 v[36:37], v[36:37], v[52:53]
	v_pk_add_f32 v[34:35], v[34:35], v[78:79] op_sel_hi:[1,0]
	v_pk_add_f32 v[36:37], v[36:37], v[78:79] op_sel_hi:[1,0]
	v_pk_fma_f32 v[34:35], v[62:63], v[76:77], v[34:35] op_sel:[0,1,0] op_sel_hi:[1,1,1]
	v_pk_fma_f32 v[36:37], v[64:65], v[76:77], v[36:37] op_sel:[0,1,0] op_sel_hi:[1,1,1]
	v_pk_add_f32 v[18:19], v[18:19], v[34:35]
	v_pk_fma_f32 v[20:21], v[34:35], v[34:35], v[20:21]
	v_pk_add_f32 v[18:19], v[18:19], v[36:37]
	v_pk_fma_f32 v[20:21], v[36:37], v[36:37], v[20:21]
	s_waitcnt lgkmcnt(2)
	v_pk_add_f32 v[38:39], v[38:39], v[54:55]
	v_pk_add_f32 v[40:41], v[40:41], v[56:57]
	v_pk_add_f32 v[38:39], v[38:39], v[78:79] op_sel_hi:[1,0]
	v_pk_add_f32 v[40:41], v[40:41], v[78:79] op_sel_hi:[1,0]
	v_pk_fma_f32 v[38:39], v[68:69], v[76:77], v[38:39] op_sel:[0,1,0] op_sel_hi:[1,1,1]
	v_pk_fma_f32 v[40:41], v[70:71], v[76:77], v[40:41] op_sel:[0,1,0] op_sel_hi:[1,1,1]
	v_pk_add_f32 v[18:19], v[18:19], v[38:39]
	v_pk_fma_f32 v[20:21], v[38:39], v[38:39], v[20:21]
	v_pk_add_f32 v[18:19], v[18:19], v[40:41]
	v_pk_fma_f32 v[20:21], v[40:41], v[40:41], v[20:21]
	s_waitcnt lgkmcnt(0)
	v_pk_add_f32 v[42:43], v[42:43], v[58:59]
	v_pk_add_f32 v[44:45], v[44:45], v[60:61]
	v_pk_add_f32 v[42:43], v[42:43], v[78:79] op_sel_hi:[1,0]
	v_pk_add_f32 v[44:45], v[44:45], v[78:79] op_sel_hi:[1,0]
	v_pk_fma_f32 v[42:43], v[72:73], v[76:77], v[42:43] op_sel:[0,1,0] op_sel_hi:[1,1,1]
	v_pk_fma_f32 v[44:45], v[74:75], v[76:77], v[44:45] op_sel:[0,1,0] op_sel_hi:[1,1,1]
	v_pk_add_f32 v[18:19], v[18:19], v[42:43]
	v_pk_fma_f32 v[20:21], v[42:43], v[42:43], v[20:21]
	v_pk_add_f32 v[18:19], v[18:19], v[44:45]
	v_pk_fma_f32 v[20:21], v[44:45], v[44:45], v[20:21]
	ds_read2st64_b32 v[50:51], v221 offset0:12 offset1:13
	ds_read2st64_b32 v[52:53], v221 offset0:14 offset1:15
	ds_read2st64_b32 v[54:55], v221 offset0:16 offset1:17
	ds_read2st64_b32 v[56:57], v221 offset0:18 offset1:19
	ds_read2st64_b32 v[58:59], v221 offset0:20 offset1:21
	ds_read2st64_b32 v[60:61], v221 offset0:22 offset1:23
	ds_read2st64_b32 v[62:63], v67 offset0:48 offset1:50
	ds_read2st64_b32 v[64:65], v67 offset0:52 offset1:54
	ds_read2st64_b32 v[68:69], v67 offset0:64 offset1:66
	ds_read2st64_b32 v[70:71], v67 offset0:68 offset1:70
	ds_read2st64_b32 v[72:73], v67 offset0:80 offset1:82
	ds_read2st64_b32 v[74:75], v67 offset0:84 offset1:86
	s_barrier
	ds_read_b32 v80, v236
	s_waitcnt lgkmcnt(5)
	v_pk_add_f32 v[46:47], v[46:47], v[50:51]
	v_pk_add_f32 v[48:49], v[48:49], v[52:53]
	v_pk_add_f32 v[46:47], v[46:47], v[78:79] op_sel_hi:[1,0]
	v_pk_add_f32 v[48:49], v[48:49], v[78:79] op_sel_hi:[1,0]
	v_pk_fma_f32 v[46:47], v[62:63], v[76:77], v[46:47] op_sel:[0,1,0] op_sel_hi:[1,1,1]
	v_pk_fma_f32 v[48:49], v[64:65], v[76:77], v[48:49] op_sel:[0,1,0] op_sel_hi:[1,1,1]
	v_pk_add_f32 v[18:19], v[18:19], v[46:47]
	v_pk_fma_f32 v[20:21], v[46:47], v[46:47], v[20:21]
	v_pk_add_f32 v[18:19], v[18:19], v[48:49]
	v_pk_fma_f32 v[20:21], v[48:49], v[48:49], v[20:21]
	s_waitcnt lgkmcnt(3)
	v_pk_add_f32 v[2:3], v[2:3], v[54:55]
	v_pk_add_f32 v[4:5], v[4:5], v[56:57]
	v_pk_add_f32 v[2:3], v[2:3], v[78:79] op_sel_hi:[1,0]
	v_pk_add_f32 v[4:5], v[4:5], v[78:79] op_sel_hi:[1,0]
	v_pk_fma_f32 v[2:3], v[68:69], v[76:77], v[2:3] op_sel:[0,1,0] op_sel_hi:[1,1,1]
	v_pk_fma_f32 v[4:5], v[70:71], v[76:77], v[4:5] op_sel:[0,1,0] op_sel_hi:[1,1,1]
	v_pk_add_f32 v[18:19], v[18:19], v[2:3]
	v_pk_fma_f32 v[20:21], v[2:3], v[2:3], v[20:21]
	v_pk_add_f32 v[18:19], v[18:19], v[4:5]
	v_pk_fma_f32 v[20:21], v[4:5], v[4:5], v[20:21]
	s_waitcnt lgkmcnt(1)
	v_pk_add_f32 v[6:7], v[6:7], v[58:59]
	v_pk_add_f32 v[8:9], v[8:9], v[60:61]
	v_pk_add_f32 v[6:7], v[6:7], v[78:79] op_sel_hi:[1,0]
	v_pk_add_f32 v[8:9], v[8:9], v[78:79] op_sel_hi:[1,0]
	v_pk_fma_f32 v[6:7], v[72:73], v[76:77], v[6:7] op_sel:[0,1,0] op_sel_hi:[1,1,1]
	v_pk_fma_f32 v[8:9], v[74:75], v[76:77], v[8:9] op_sel:[0,1,0] op_sel_hi:[1,1,1]
	v_pk_add_f32 v[18:19], v[18:19], v[6:7]
	v_pk_fma_f32 v[20:21], v[6:7], v[6:7], v[20:21]
	v_pk_add_f32 v[18:19], v[18:19], v[8:9]
	v_pk_fma_f32 v[20:21], v[8:9], v[8:9], v[20:21]
	v_add_f32_e32 v18, v18, v19
	v_add_f32_e32 v20, v20, v21
	v_mov_b32_e32 v19, v18
	v_mov_b32_e32 v21, v20
	s_nop 1
	v_permlane32_swap_b32_e32 v18, v19
	v_permlane32_swap_b32_e32 v20, v21
	v_add_f32_e32 v18, v18, v19
	v_add_f32_e32 v20, v20, v21
	v_cndmask_b32_e64 v22, v20, v18, s[0:1]
	s_branch .Lep2_wr0
.Lep2_k1:
	s_setprio 2
	v_mov_b32_e32 v34, 0
	v_mov_b32_e32 v35, 0
	v_mov_b32_e32 v36, 0
	v_mov_b32_e32 v37, 0
	ds_read2st64_b32 v[50:51], v221 offset0:24 offset1:25
	ds_read2st64_b32 v[52:53], v221 offset0:26 offset1:27
	ds_read2st64_b32 v[54:55], v221 offset0:28 offset1:29
	ds_read2st64_b32 v[56:57], v221 offset0:30 offset1:31
	ds_read2st64_b32 v[58:59], v221 offset0:32 offset1:33
	ds_read2st64_b32 v[60:61], v221 offset0:34 offset1:35
	ds_read2st64_b32 v[62:63], v67 offset0:96 offset1:98
	ds_read2st64_b32 v[64:65], v67 offset0:100 offset1:102
	ds_read2st64_b32 v[68:69], v67 offset0:112 offset1:114
	ds_read2st64_b32 v[70:71], v67 offset0:116 offset1:118
	ds_read2st64_b32 v[72:73], v67 offset0:128 offset1:130
	ds_read2st64_b32 v[74:75], v67 offset0:132 offset1:134
	s_waitcnt lgkmcnt(12)
	v_fma_f32 v78, -v76, v77, v173
	s_waitcnt lgkmcnt(4)
	v_pk_add_f32 v[10:11], v[10:11], v[50:51]
	v_pk_add_f32 v[12:13], v[12:13], v[52:53]
	v_pk_add_f32 v[10:11], v[10:11], v[78:79] op_sel_hi:[1,0]
	v_pk_add_f32 v[12:13], v[12:13], v[78:79] op_sel_hi:[1,0]
	v_pk_fma_f32 v[10:11], v[62:63], v[76:77], v[10:11] op_sel:[0,1,0] op_sel_hi:[1,1,1]
	v_pk_fma_f32 v[12:13], v[64:65], v[76:77], v[12:13] op_sel:[0,1,0] op_sel_hi:[1,1,1]
	v_pk_add_f32 v[34:35], v[34:35], v[10:11]
	v_pk_fma_f32 v[36:37], v[10:11], v[10:11], v[36:37]
	v_pk_add_f32 v[34:35], v[34:35], v[12:13]
	v_pk_fma_f32 v[36:37], v[12:13], v[12:13], v[36:37]
	s_waitcnt lgkmcnt(2)
	v_pk_add_f32 v[14:15], v[14:15], v[54:55]
	v_pk_add_f32 v[16:17], v[16:17], v[56:57]
	v_pk_add_f32 v[14:15], v[14:15], v[78:79] op_sel_hi:[1,0]
	v_pk_add_f32 v[16:17], v[16:17], v[78:79] op_sel_hi:[1,0]
	v_pk_fma_f32 v[14:15], v[68:69], v[76:77], v[14:15] op_sel:[0,1,0] op_sel_hi:[1,1,1]
	v_pk_fma_f32 v[16:17], v[70:71], v[76:77], v[16:17] op_sel:[0,1,0] op_sel_hi:[1,1,1]
	v_pk_add_f32 v[34:35], v[34:35], v[14:15]
	v_pk_fma_f32 v[36:37], v[14:15], v[14:15], v[36:37]
	v_pk_add_f32 v[34:35], v[34:35], v[16:17]
	v_pk_fma_f32 v[36:37], v[16:17], v[16:17], v[36:37]
	s_waitcnt lgkmcnt(0)
	v_pk_add_f32 v[18:19], v[18:19], v[58:59]
	v_pk_add_f32 v[20:21], v[20:21], v[60:61]
	v_pk_add_f32 v[18:19], v[18:19], v[78:79] op_sel_hi:[1,0]
	v_pk_add_f32 v[20:21], v[20:21], v[78:79] op_sel_hi:[1,0]
	v_pk_fma_f32 v[18:19], v[72:73], v[76:77], v[18:19] op_sel:[0,1,0] op_sel_hi:[1,1,1]
	v_pk_fma_f32 v[20:21], v[74:75], v[76:77], v[20:21] op_sel:[0,1,0] op_sel_hi:[1,1,1]
	v_pk_add_f32 v[34:35], v[34:35], v[18:19]
	v_pk_fma_f32 v[36:37], v[18:19], v[18:19], v[36:37]
	v_pk_add_f32 v[34:35], v[34:35], v[20:21]
	v_pk_fma_f32 v[36:37], v[20:21], v[20:21], v[36:37]
	ds_read2st64_b32 v[50:51], v221 offset0:36 offset1:37
	ds_read2st64_b32 v[52:53], v221 offset0:38 offset1:39
	ds_read2st64_b32 v[62:63], v67 offset0:144 offset1:146
	ds_read2st64_b32 v[64:65], v67 offset0:148 offset1:150
	s_waitcnt lgkmcnt(0)
	v_pk_add_f32 v[22:23], v[22:23], v[50:51]
	v_pk_add_f32 v[24:25], v[24:25], v[52:53]
	v_pk_add_f32 v[22:23], v[22:23], v[78:79] op_sel_hi:[1,0]
	v_pk_add_f32 v[24:25], v[24:25], v[78:79] op_sel_hi:[1,0]
	v_pk_fma_f32 v[22:23], v[62:63], v[76:77], v[22:23] op_sel:[0,1,0] op_sel_hi:[1,1,1]
	v_pk_fma_f32 v[24:25], v[64:65], v[76:77], v[24:25] op_sel:[0,1,0] op_sel_hi:[1,1,1]
	v_pk_add_f32 v[34:35], v[34:35], v[22:23]
	v_pk_fma_f32 v[36:37], v[22:23], v[22:23], v[36:37]
	v_pk_add_f32 v[34:35], v[34:35], v[24:25]
	v_pk_fma_f32 v[36:37], v[24:25], v[24:25], v[36:37]
	s_mov_b64 s[40:41], exec
	s_and_b64 exec, exec, s[0:1]
	ds_read2st64_b32 v[50:51], v221 offset0:40 offset1:41
	ds_read2st64_b32 v[52:53], v221 offset0:42 offset1:43
	ds_read2st64_b32 v[62:63], v67 offset0:160 offset1:162
	ds_read2st64_b32 v[64:65], v67 offset0:164 offset1:166
	s_waitcnt lgkmcnt(0)
	v_pk_add_f32 v[26:27], v[26:27], v[50:51]
	v_pk_add_f32 v[28:29], v[28:29], v[52:53]
	v_pk_add_f32 v[26:27], v[26:27], v[78:79] op_sel_hi:[1,0]
	v_pk_add_f32 v[28:29], v[28:29], v[78:79] op_sel_hi:[1,0]
	v_pk_fma_f32 v[26:27], v[62:63], v[76:77], v[26:27] op_sel:[0,1,0] op_sel_hi:[1,1,1]
	v_pk_fma_f32 v[28:29], v[64:65], v[76:77], v[28:29] op_sel:[0,1,0] op_sel_hi:[1,1,1]
	v_pk_add_f32 v[34:35], v[34:35], v[26:27]
	v_pk_fma_f32 v[36:37], v[26:27], v[26:27], v[36:37]
	v_pk_add_f32 v[34:35], v[34:35], v[28:29]
	v_pk_fma_f32 v[36:37], v[28:29], v[28:29], v[36:37]
	s_mov_b64 exec, s[40:41]
	v_add_f32_e32 v34, v34, v35
	v_add_f32_e32 v36, v36, v37
	v_mov_b32_e32 v35, v34
	v_mov_b32_e32 v37, v36
	s_nop 1
	v_permlane32_swap_b32_e32 v34, v35
	v_permlane32_swap_b32_e32 v36, v37
	v_add_f32_e32 v34, v34, v35
	v_add_f32_e32 v36, v36, v37
	v_cndmask_b32_e64 v38, v36, v34, s[0:1]
	ds_write_b32 v236, v38

.Lep2_wr0:
	s_mul_i32 s43, s36, 0x5000
	s_addk_i32 s43, 0x2800
	s_add_i32 s43, s43, s86
	s_add_u32 s40, s18, s43
	s_addc_u32 s41, s19, 0
	s_waitcnt lgkmcnt(0)
	v_add_f32_e32 v22, v22, v80
	v_mov_b32_e32 v59, v22
	v_cndmask_b32_e64 v57, v22, 1.0, s[84:85]
	v_writelane_b32 v59, 1.0, 0
	s_mov_b64 s[44:45], exec
	s_mov_b32 exec_lo, -1
	s_mov_b32 exec_hi, 0xfffffff
	global_atomic_add_f32 v253, v57, s[40:41]
	s_mov_b32 exec_lo, 0xf0000001
	s_mov_b32 exec_hi, 0xf0000000
	global_atomic_add_f32 v254, v59, s[40:41]
	s_mov_b64 exec, s[44:45]
	ds_write2st64_b32 v67, v34, v35 offset0:0 offset1:2
	ds_write2st64_b32 v67, v36, v37 offset0:4 offset1:6
	ds_write2st64_b32 v67, v38, v39 offset0:16 offset1:18
	ds_write2st64_b32 v67, v40, v41 offset0:20 offset1:22
	ds_write2st64_b32 v67, v42, v43 offset0:32 offset1:34
	ds_write2st64_b32 v67, v44, v45 offset0:36 offset1:38
	ds_write2st64_b32 v67, v46, v47 offset0:48 offset1:50
	ds_write2st64_b32 v67, v48, v49 offset0:52 offset1:54
	ds_write2st64_b32 v67, v2, v3 offset0:64 offset1:66
	ds_write2st64_b32 v67, v4, v5 offset0:68 offset1:70
	ds_write2st64_b32 v67, v6, v7 offset0:80 offset1:82
	ds_write2st64_b32 v67, v8, v9 offset0:84 offset1:86
	s_branch .Lep2_end
